# P + attention: next segment's K fragments prefetched in the MFMA shadows (2 ds_read_b128 behind each of the 4 P.V MFMAs) of the previous MFMA segment into spare VGPRs v222-253; removed from the softma
# speedup vs baseline: 1.0156x; 1.0156x over previous
.LBB0_1614:
	s_mul_i32 s14, s13, 0x3400
	s_and_b32 s7, 1, s18
	s_add_i32 s14, s14, 0
	s_andn2_b32 s15, 1, s18
	s_mul_i32 s6, s17, 0x3400
	s_cmpk_lt_u32 s18, 0xfc
	s_cselect_b32 s21, s20, 0x2fd000
	s_cmp_eq_u32 s7, 1
	v_add_u32_e32 v96, s14, v199
	s_waitcnt lgkmcnt(6)
	v_mfma_scale_f32_32x32x64_f8f6f4 v[80:95], v[222:229], v[136:143], v[64:79], v191, v190 op_sel_hi:[0,0,0]
	s_waitcnt vmcnt(2)
	ds_write_b128 v96, v[180:183] offset:20480
	v_add_u32_e32 v96, s14, v200
	s_mulk_i32 s15, 0x2800
	s_waitcnt vmcnt(1)
	ds_write_b64 v96, v[188:189] offset:28672
	v_add_u32_e32 v96, s15, v205
	s_mov_b32 s39, s31
	s_waitcnt vmcnt(0)
	ds_write_b128 v96, v[176:179]
	buffer_load_dwordx4 v[180:183], v203, s[28:31], s21 offen
	buffer_load_dwordx2 v[188:189], v202, s[28:31], s21 offen
	buffer_load_dwordx4 v[176:179], v203, s[36:39], s19 offen
	v_add_u32_e32 v172, s6, v204
	s_cselect_b32 s6, 0x2800, 0
	v_add_u32_e32 v186, s6, v198
	s_waitcnt lgkmcnt(7)
	v_mfma_scale_f32_32x32x64_f8f6f4 v[96:111], v[230:237], v[136:143], v[64:79], v191, v190 op_sel_hi:[0,0,0]
	ds_read_b128 v[160:163], v172 offset:20608
	ds_read_b128 v[164:167], v172 offset:20624
	ds_read_b128 v[168:171], v172 offset:27264
	ds_read_b128 v[172:175], v172 offset:27280
	s_waitcnt lgkmcnt(9)
	v_mfma_scale_f32_32x32x64_f8f6f4 v[80:95], v[238:245], v[128:135], v[80:95], v191, v190 op_sel_hi:[0,0,0]
	ds_read_b128 v[152:155], v186
	ds_read_b128 v[156:159], v186 offset:16
	ds_read_b128 v[206:209], v186 offset:2560
	ds_read_b128 v[210:213], v186 offset:2576
	s_waitcnt lgkmcnt(11)
	v_mfma_scale_f32_32x32x64_f8f6f4 v[96:111], v[246:253], v[128:135], v[96:111], v191, v190 op_sel_hi:[0,0,0]
	ds_read_b128 v[144:147], v186 offset:5120
	ds_read_b128 v[148:151], v186 offset:5136
	ds_read_b128 v[214:217], v186 offset:7680
	ds_read_b128 v[218:221], v186 offset:7696
	s_waitcnt lgkmcnt(10)
	v_mfma_scale_f32_32x32x64_f8f6f4 v[80:95], v[160:167], v[120:127], v[80:95], v191, v190 op_sel_hi:[0,0,0]
	s_waitcnt lgkmcnt(8)
	v_mfma_scale_f32_32x32x64_f8f6f4 v[96:111], v[168:175], v[120:127], v[96:111], v191, v190 op_sel_hi:[0,0,0]
	s_mul_i32 s14, s16, 0x3400
	v_add_u32_e32 v254, s14, v204
	s_waitcnt lgkmcnt(6)
	v_mfma_f32_32x32x64_f8f6f4 v[0:15], v[112:119], v[152:159], v[0:15]
	ds_read_b128 v[222:225], v254 offset:20480
	ds_read_b128 v[226:229], v254 offset:20496
	s_waitcnt lgkmcnt(6)
	v_mfma_f32_32x32x64_f8f6f4 v[16:31], v[112:119], v[206:213], v[16:31]
	ds_read_b128 v[230:233], v254 offset:27136
	ds_read_b128 v[234:237], v254 offset:27152
	s_waitcnt lgkmcnt(6)
	v_mfma_f32_32x32x64_f8f6f4 v[32:47], v[112:119], v[144:151], v[32:47]
	ds_read_b128 v[238:241], v254 offset:20544
	ds_read_b128 v[242:245], v254 offset:20560
	s_waitcnt lgkmcnt(6)
	v_mfma_f32_32x32x64_f8f6f4 v[48:63], v[112:119], v[214:221], v[48:63]
	ds_read_b128 v[246:249], v254 offset:27200
	ds_read_b128 v[250:253], v254 offset:27216
	v_cndmask_b32_e64 v144, 0, 1, s[46:47]
	v_cmp_ne_u32_e64 s[6:7], 1, v144
	s_andn2_b64 vcc, exec, s[46:47]
	s_cbranch_vccnz .LBB0_1616
	s_barrier
